# speedup vs baseline: 1.0050x; 1.0050x over previous
_Z6gemm_pILi2ELi8EEvPKDF16_S1_iiiiiiPKfS3_S3_PfPDF16_S4_S5_S4_:
	s_load_dword s3, s[0:1], 0x10
	s_load_dword s4, s[0:1], 0x68
	s_load_dwordx4 s[12:15], s[0:1], 0x0
	s_load_dword s20, s[0:1], 0x24
	s_load_dwordx2 s[8:9], s[0:1], 0x18
	s_waitcnt lgkmcnt(0)
	s_ashr_i32 s21, s3, 7
	s_ashr_i32 s25, s3, 31
	s_abs_i32 s24, s21
	s_lshr_b32 s22, s4, 3
	s_and_b32 s4, s2, 7
	s_mul_i32 s4, s20, s4
	s_mul_i32 s4, s4, s22
	s_lshr_b32 s2, s2, 3
	s_add_i32 s23, s4, s2
	s_ff1_i32_b32 s44, s21
	s_lshr_b32 s2, s23, s44
	s_lshl_b32 s4, s2, 7
	s_mul_i32 s2, s2, s21
	s_sub_i32 s2, s23, s2
	s_lshl_b32 s16, s2, 7
	s_mul_hi_i32 s3, s4, s8
	s_mul_i32 s2, s4, s8
	s_lshl_b64 s[2:3], s[2:3], 1
	s_add_u32 s4, s12, s2
	s_addc_u32 s2, s13, s3
	s_and_b32 s5, s2, 0xffff
	s_mul_hi_i32 s3, s16, s9
	s_mul_i32 s2, s16, s9
	s_lshl_b64 s[2:3], s[2:3], 1
	s_add_u32 s12, s14, s2
	s_addc_u32 s2, s15, s3
	v_lshrrev_b32_e32 v1, 4, v0
	s_and_b32 s13, s2, 0xffff
	v_readfirstlane_b32 s2, v0
	v_xor_b32_e32 v4, v1, v0
	s_lshl_b32 s2, s2, 4
	v_lshrrev_b32_e32 v2, 3, v0
	v_lshlrev_b32_e32 v4, 3, v4
	s_and_b32 s2, s2, 0xfffffc00
	v_and_b32_e32 v4, 56, v4
	s_mov_b32 s11, 0x20000
	s_mov_b32 s10, 0x7ffffff0
	v_mul_lo_u32 v3, s8, v2
	s_add_i32 s2, s2, 0
	s_mov_b32 s6, s10
	s_mov_b32 s7, s11
	v_add_lshl_u32 v72, v3, v4, 1
	s_mov_b32 m0, s2
	v_mul_lo_u32 v2, s9, v2
	buffer_load_dwordx4 v72, s[4:7], 0 offen lds
	s_add_i32 m0, s2, 0x2000
	v_lshl_add_u32 v74, s8, 7, v72
	s_mov_b32 s14, s10
	s_mov_b32 s15, s11
	v_add_lshl_u32 v73, v2, v4, 1
	buffer_load_dwordx4 v74, s[4:7], 0 offen lds
	s_add_i32 m0, s2, 0x4000
	v_lshl_add_u32 v75, s9, 7, v73
	buffer_load_dwordx4 v73, s[12:15], 0 offen lds
	s_add_i32 m0, s2, 0x6000
	s_movk_i32 s3, 0x80
	buffer_load_dwordx4 v75, s[12:15], 0 offen lds
	s_add_i32 m0, s2, 0x8000
	s_mov_b32 s27, 3
	buffer_load_dwordx4 v72, s[4:7], s3 offen lds
	s_add_i32 m0, s2, 0xa000
	s_nop 0
	buffer_load_dwordx4 v74, s[4:7], s3 offen lds
	s_add_i32 m0, s2, 0xc000
	s_nop 0
	buffer_load_dwordx4 v73, s[12:15], s3 offen lds
	s_add_i32 m0, s2, 0xe000
	s_nop 0
	buffer_load_dwordx4 v75, s[12:15], s3 offen lds
	s_add_i32 m0, s2, 0x10000
	s_movk_i32 s3, 0x100
	buffer_load_dwordx4 v72, s[4:7], s3 offen lds
	s_add_i32 m0, s2, 0x12000
	s_nop 0
	buffer_load_dwordx4 v74, s[4:7], s3 offen lds
	s_add_i32 m0, s2, 0x14000
	s_nop 0
	buffer_load_dwordx4 v73, s[12:15], s3 offen lds
	s_add_i32 m0, s2, 0x16000
	s_cmp_lt_i32 s20, 1
	buffer_load_dwordx4 v75, s[12:15], s3 offen lds
	s_cbranch_scc1 .LBB7_11
	v_cvt_f32_u32_e32 v3, s24
	s_sub_i32 s44, 0, s24
	v_rcp_iflag_f32_e32 v3, v3
	s_nop 0
	v_mul_f32_e32 v3, 0x4f7ffffe, v3
	v_cvt_u32_f32_e32 v3, v3
	s_nop 0
	v_readfirstlane_b32 s26, v3
	s_mul_i32 s44, s44, s26
	s_mul_hi_u32 s44, s26, s44
	s_add_i32 s26, s26, s44
	v_lshrrev_b32_e32 v2, 8, v0
	s_load_dwordx4 s[16:19], s[0:1], 0x48
	s_load_dwordx2 s[2:3], s[0:1], 0x30
	v_lshlrev_b32_e32 v3, 2, v2
	v_bfe_u32 v4, v0, 5, 1
	v_bfe_u32 v7, v0, 1, 3
	v_or_b32_e32 v5, v3, v4
	v_bitop3_b32 v3, v3, v7, v4 bitop3:0x36
	v_bitop3_b32 v5, v5, v7, 2 bitop3:0x36
	v_lshlrev_b32_e32 v77, 4, v3
	v_lshlrev_b32_e32 v3, 7, v0
	v_lshrrev_b32_e32 v6, 1, v0
	v_lshlrev_b32_e32 v76, 4, v5
	v_and_b32_e32 v5, 0x2f80, v3
	v_and_b32_e32 v3, 31, v0
	v_and_b32_e32 v12, 15, v0
	v_mov_b32_e32 v66, 0
	v_and_or_b32 v6, v6, 64, v3
	v_lshlrev_b32_e32 v10, 16, v2
	v_lshlrev_b32_e32 v2, 5, v12
	v_mov_b32_e32 v3, v66
	s_waitcnt lgkmcnt(0)
	v_lshl_add_u64 v[68:69], s[2:3], 0, v[2:3]
	v_lshlrev_b32_e32 v2, 4, v12
	v_and_b32_e32 v8, 64, v0
	v_lshl_add_u64 v[70:71], s[16:17], 0, v[2:3]
	v_lshlrev_b32_e32 v2, 1, v12
	v_or_b32_e32 v3, 1, v2
	v_lshrrev_b32_e32 v8, 2, v8
	v_lshlrev_b32_e32 v9, 7, v6
	v_and_b32_e32 v11, 7, v0
	v_or_b32_e32 v14, v8, v4
	v_lshlrev_b32_e32 v6, 9, v6
	v_bitop3_b32 v2, v1, v2, 7 bitop3:0x6c
	v_bitop3_b32 v3, v1, v3, 7 bitop3:0x6c
	v_add3_u32 v6, 0, v10, v6
	v_bitop3_b32 v4, v8, v11, v4 bitop3:0x36
	v_bitop3_b32 v8, v14, v11, 2 bitop3:0x36
	v_bitop3_b32 v10, v14, v11, 4 bitop3:0x36
	v_bitop3_b32 v15, v14, v11, 6 bitop3:0x36
	v_bitop3_b32 v16, v14, v11, 8 bitop3:0x36
	v_bitop3_b32 v17, v14, v11, 10 bitop3:0x36
	v_bitop3_b32 v18, v14, v11, 12 bitop3:0x36
	v_bitop3_b32 v11, v14, v11, 14 bitop3:0x36
	v_lshlrev_b32_e32 v14, 9, v1
	v_lshlrev_b32_e32 v2, 4, v2
	v_lshlrev_b32_e32 v3, 4, v3
	v_or_b32_e32 v87, 32, v1
	v_or_b32_e32 v85, v2, v14
	v_or_b32_e32 v86, v3, v14
	v_lshlrev_b32_e32 v14, 9, v87
	v_or_b32_e32 v90, 64, v1
	v_or_b32_e32 v88, v2, v14
	v_or_b32_e32 v89, v3, v14
	v_lshlrev_b32_e32 v14, 9, v90
	v_or_b32_e32 v93, 0x60, v1
	s_add_i32 s28, 0, 0x10000
	s_add_i32 s0, 0, 0x18000
	v_or_b32_e32 v91, v2, v14
	v_or_b32_e32 v92, v3, v14
	v_lshlrev_b32_e32 v14, 9, v93
	v_or_b32_e32 v7, 0x4000, v5
	v_lshlrev_b32_e32 v78, 3, v12
	v_cmp_eq_u32_e32 vcc, 0, v12
	v_add_u32_e32 v79, 0, v9
	v_add_u32_e32 v80, 0, v5
	v_add_u32_e32 v81, s28, v9
	v_add_u32_e32 v5, s28, v77
	v_add_u32_e32 v12, s28, v76
	v_add_u32_e32 v83, s0, v9
	v_add_u32_e32 v9, s0, v77
	v_add_u32_e32 v13, s0, v76
	v_lshlrev_b32_e32 v4, 4, v4
	v_lshlrev_b32_e32 v8, 4, v8
	v_lshlrev_b32_e32 v10, 4, v10
	v_lshlrev_b32_e32 v15, 4, v15
	v_lshlrev_b32_e32 v16, 4, v16
	v_lshlrev_b32_e32 v17, 4, v17
	v_lshlrev_b32_e32 v18, 4, v18
	v_lshlrev_b32_e32 v11, 4, v11
	v_or_b32_e32 v94, v2, v14
	v_mbcnt_lo_u32_b32 v2, -1, 0
	s_and_b32 s9, s17, 0xffff
	s_mov_b32 s8, s16
	s_and_b32 s17, s19, 0xffff
	s_mov_b32 s16, s18
	v_add_u32_e32 v82, s28, v7
	v_add_u32_e32 v84, s0, v7
	v_or_b32_e32 v95, v3, v14
	s_movk_i32 s0, 0x180
	v_add_u32_e32 v96, v5, v7
	v_add_u32_e32 v97, v12, v7
	v_add_u32_e32 v98, v9, v7
	v_add_u32_e32 v99, v13, v7
	v_add_u32_e32 v100, v6, v4
	v_add_u32_e32 v101, v6, v8
	v_add_u32_e32 v102, v6, v10
	v_add_u32_e32 v103, v6, v15
	v_add_u32_e32 v104, v6, v16
	v_add_u32_e32 v105, v6, v17
	v_add_u32_e32 v106, v6, v18
	v_add_u32_e32 v107, v6, v11
	s_movk_i32 s29, 0x480
	v_mbcnt_hi_u32_b32 v108, -1, v2
	s_movk_i32 s30, 0x240
	s_mov_b32 s6, s10
	s_mov_b32 s7, s11
	s_branch .LBB7_3

_Z6gemm_pILi2ELi32EEvPKDF16_S1_iiiiiiPKfS3_S3_PfPDF16_S4_S5_S4_:
	s_load_dword s3, s[0:1], 0x10
	s_load_dword s4, s[0:1], 0x68
	s_load_dwordx4 s[12:15], s[0:1], 0x0
	s_load_dword s20, s[0:1], 0x24
	s_load_dwordx2 s[8:9], s[0:1], 0x18
	s_waitcnt lgkmcnt(0)
	s_ashr_i32 s21, s3, 7
	s_ashr_i32 s25, s3, 31
	s_abs_i32 s24, s21
	s_lshr_b32 s22, s4, 3
	s_and_b32 s4, s2, 7
	s_mul_i32 s4, s20, s4
	s_mul_i32 s4, s4, s22
	s_lshr_b32 s2, s2, 3
	s_add_i32 s23, s4, s2
	s_ff1_i32_b32 s44, s21
	s_lshr_b32 s2, s23, s44
	s_lshl_b32 s4, s2, 7
	s_mul_i32 s2, s2, s21
	s_sub_i32 s2, s23, s2
	s_lshl_b32 s16, s2, 7
	s_mul_hi_i32 s3, s4, s8
	s_mul_i32 s2, s4, s8
	s_lshl_b64 s[2:3], s[2:3], 1
	s_add_u32 s4, s12, s2
	s_addc_u32 s2, s13, s3
	s_and_b32 s5, s2, 0xffff
	s_mul_hi_i32 s3, s16, s9
	s_mul_i32 s2, s16, s9
	s_lshl_b64 s[2:3], s[2:3], 1
	s_add_u32 s12, s14, s2
	s_addc_u32 s2, s15, s3
	v_lshrrev_b32_e32 v1, 4, v0
	s_and_b32 s13, s2, 0xffff
	v_readfirstlane_b32 s2, v0
	v_xor_b32_e32 v4, v1, v0
	s_lshl_b32 s2, s2, 4
	v_lshrrev_b32_e32 v2, 3, v0
	v_lshlrev_b32_e32 v4, 3, v4
	s_and_b32 s2, s2, 0xfffffc00
	v_and_b32_e32 v4, 56, v4
	s_mov_b32 s11, 0x20000
	s_mov_b32 s10, 0x7ffffff0
	v_mul_lo_u32 v3, s8, v2
	s_add_i32 s2, s2, 0
	s_mov_b32 s6, s10
	s_mov_b32 s7, s11
	v_add_lshl_u32 v72, v3, v4, 1
	s_mov_b32 m0, s2
	v_mul_lo_u32 v2, s9, v2
	buffer_load_dwordx4 v72, s[4:7], 0 offen lds
	s_add_i32 m0, s2, 0x2000
	v_lshl_add_u32 v74, s8, 7, v72
	s_mov_b32 s14, s10
	s_mov_b32 s15, s11
	v_add_lshl_u32 v73, v2, v4, 1
	buffer_load_dwordx4 v74, s[4:7], 0 offen lds
	s_add_i32 m0, s2, 0x4000
	v_lshl_add_u32 v75, s9, 7, v73
	buffer_load_dwordx4 v73, s[12:15], 0 offen lds
	s_add_i32 m0, s2, 0x6000
	s_movk_i32 s3, 0x80
	buffer_load_dwordx4 v75, s[12:15], 0 offen lds
	s_add_i32 m0, s2, 0x8000
	s_mov_b32 s27, 3
	buffer_load_dwordx4 v72, s[4:7], s3 offen lds
	s_add_i32 m0, s2, 0xa000
	s_nop 0
	buffer_load_dwordx4 v74, s[4:7], s3 offen lds
	s_add_i32 m0, s2, 0xc000
	s_nop 0
	buffer_load_dwordx4 v73, s[12:15], s3 offen lds
	s_add_i32 m0, s2, 0xe000
	s_nop 0
	buffer_load_dwordx4 v75, s[12:15], s3 offen lds
	s_add_i32 m0, s2, 0x10000
	s_movk_i32 s3, 0x100
	buffer_load_dwordx4 v72, s[4:7], s3 offen lds
	s_add_i32 m0, s2, 0x12000
	s_nop 0
	buffer_load_dwordx4 v74, s[4:7], s3 offen lds
	s_add_i32 m0, s2, 0x14000
	s_nop 0
	buffer_load_dwordx4 v73, s[12:15], s3 offen lds
	s_add_i32 m0, s2, 0x16000
	s_cmp_lt_i32 s20, 1
	buffer_load_dwordx4 v75, s[12:15], s3 offen lds
	s_cbranch_scc1 .LBB9_11
	v_cvt_f32_u32_e32 v3, s24
	s_sub_i32 s44, 0, s24
	v_rcp_iflag_f32_e32 v3, v3
	s_nop 0
	v_mul_f32_e32 v3, 0x4f7ffffe, v3
	v_cvt_u32_f32_e32 v3, v3
	s_nop 0
	v_readfirstlane_b32 s26, v3
	s_mul_i32 s44, s44, s26
	s_mul_hi_u32 s44, s26, s44
	s_add_i32 s26, s26, s44
	s_load_dwordx4 s[16:19], s[0:1], 0x48
	s_load_dwordx2 s[2:3], s[0:1], 0x30
	v_lshrrev_b32_e32 v2, 8, v0
	v_lshrrev_b32_e32 v3, 1, v0
	v_and_b32_e32 v8, 31, v0
	v_and_b32_e32 v12, 15, v0
	v_mov_b32_e32 v66, 0
	v_bfe_u32 v4, v0, 5, 1
	v_lshlrev_b32_e32 v6, 2, v2
	v_and_or_b32 v8, v3, 64, v8
	v_lshlrev_b32_e32 v10, 16, v2
	v_lshlrev_b32_e32 v2, 5, v12
	v_mov_b32_e32 v3, v66
	v_bfe_u32 v5, v0, 1, 3
	v_or_b32_e32 v7, v6, v4
	s_waitcnt lgkmcnt(0)
	v_lshl_add_u64 v[68:69], s[2:3], 0, v[2:3]
	v_lshlrev_b32_e32 v2, 4, v12
	v_bitop3_b32 v6, v6, v5, v4 bitop3:0x36
	v_bitop3_b32 v5, v7, v5, 2 bitop3:0x36
	v_and_b32_e32 v7, 64, v0
	v_lshl_add_u64 v[70:71], s[16:17], 0, v[2:3]
	v_lshlrev_b32_e32 v2, 1, v12
	v_or_b32_e32 v3, 1, v2
	v_lshrrev_b32_e32 v7, 2, v7
	v_lshlrev_b32_e32 v9, 7, v8
	v_and_b32_e32 v11, 7, v0
	v_or_b32_e32 v14, v7, v4
	v_lshlrev_b32_e32 v8, 9, v8
	v_bitop3_b32 v2, v1, v2, 7 bitop3:0x6c
	v_bitop3_b32 v3, v1, v3, 7 bitop3:0x6c
	v_add3_u32 v8, 0, v10, v8
	v_bitop3_b32 v4, v7, v11, v4 bitop3:0x36
	v_bitop3_b32 v7, v14, v11, 2 bitop3:0x36
	v_bitop3_b32 v10, v14, v11, 4 bitop3:0x36
	v_bitop3_b32 v15, v14, v11, 6 bitop3:0x36
	v_bitop3_b32 v16, v14, v11, 8 bitop3:0x36
	v_bitop3_b32 v17, v14, v11, 10 bitop3:0x36
	v_bitop3_b32 v18, v14, v11, 12 bitop3:0x36
	v_bitop3_b32 v11, v14, v11, 14 bitop3:0x36
	v_lshlrev_b32_e32 v14, 9, v1
	v_lshlrev_b32_e32 v2, 4, v2
	v_lshlrev_b32_e32 v3, 4, v3
	v_or_b32_e32 v87, 32, v1
	v_or_b32_e32 v85, v2, v14
	v_or_b32_e32 v86, v3, v14
	v_lshlrev_b32_e32 v14, 9, v87
	v_or_b32_e32 v90, 64, v1
	v_lshlrev_b32_e32 v77, 4, v5
	v_lshlrev_b32_e32 v5, 7, v0
	v_or_b32_e32 v88, v2, v14
	v_or_b32_e32 v89, v3, v14
	v_lshlrev_b32_e32 v14, 9, v90
	v_or_b32_e32 v93, 0x60, v1
	v_lshlrev_b32_e32 v76, 4, v6
	v_and_b32_e32 v5, 0x2f80, v5
	s_add_i32 s28, 0, 0x10000
	s_add_i32 s0, 0, 0x18000
	v_or_b32_e32 v91, v2, v14
	v_or_b32_e32 v92, v3, v14
	v_lshlrev_b32_e32 v14, 9, v93
	v_or_b32_e32 v6, 0x4000, v5
	v_lshlrev_b32_e32 v78, 3, v12
	v_cmp_eq_u32_e32 vcc, 0, v12
	v_add_u32_e32 v79, 0, v9
	v_add_u32_e32 v80, 0, v5
	v_add_u32_e32 v81, s28, v9
	v_add_u32_e32 v5, s28, v76
	v_add_u32_e32 v12, s28, v77
	v_add_u32_e32 v83, s0, v9
	v_add_u32_e32 v9, s0, v76
	v_add_u32_e32 v13, s0, v77
	v_lshlrev_b32_e32 v4, 4, v4
	v_lshlrev_b32_e32 v7, 4, v7
	v_lshlrev_b32_e32 v10, 4, v10
	v_lshlrev_b32_e32 v15, 4, v15
	v_lshlrev_b32_e32 v16, 4, v16
	v_lshlrev_b32_e32 v17, 4, v17
	v_lshlrev_b32_e32 v18, 4, v18
	v_lshlrev_b32_e32 v11, 4, v11
	v_or_b32_e32 v94, v2, v14
	v_mbcnt_lo_u32_b32 v2, -1, 0
	s_and_b32 s9, s17, 0xffff
	s_mov_b32 s8, s16
	s_and_b32 s17, s19, 0xffff
	s_mov_b32 s16, s18
	v_add_u32_e32 v82, s28, v6
	v_add_u32_e32 v84, s0, v6
	v_or_b32_e32 v95, v3, v14
	s_movk_i32 s0, 0x180
	v_add_u32_e32 v96, v5, v6
	v_add_u32_e32 v97, v12, v6
	v_add_u32_e32 v98, v9, v6
	v_add_u32_e32 v99, v13, v6
	s_movk_i32 s29, 0x480
	v_add_u32_e32 v100, v8, v4
	v_add_u32_e32 v101, v8, v7
	v_add_u32_e32 v102, v8, v10
	v_add_u32_e32 v103, v8, v15
	v_add_u32_e32 v104, v8, v16
	v_add_u32_e32 v105, v8, v17
	v_add_u32_e32 v106, v8, v18
	v_add_u32_e32 v107, v8, v11
	v_mbcnt_hi_u32_b32 v108, -1, v2
	s_movk_i32 s30, 0x240
	s_mov_b32 s6, s10
	s_mov_b32 s7, s11
	s_branch .LBB9_3
